# attention: static priority raise for waves 4-7 (the second wave of each SIMD) during the attention units (on v11)
# baseline (speedup 1.0000x reference)
; __device__ __forceinline__ void ph_attn_carry(const Params& p, int l, LAS unsigned char* lds) {
;     ...
;     for (int it = blockIdx.x; it < natt; it += gridDim.x) {
;         {
;             int b, h, row0, nkeys;
;             if (it < 256) { const int x = it & 7, jj = it >> 3, bh = 2 * x + (jj >> 4); b = bh >> 2; h = bh & 3; row0 = b * SEQ + (jj & 15) * 128; nkeys = NKEY; }
;             else { const int u = it - 256; b = u >> 3; h = (u >> 1) & 3; row0 = NLAT + b * CTX + (u & 1) * 128; nkeys = CTX; }
;             attn_unit(QB + (size_t)row0 * 768 + h * 192, KC + (size_t)(b * 4 + h) * NKEY * 192, VT + (size_t)(b * 4 + h) * 128 * NKEY, nkeys, CAT + (size_t)row0 * DM + 512 + h * 128, lds);
.LBB0_1229:
	v_readfirstlane_b32 s96, v0
	s_cmpk_gt_u32 s96, 0xff
	s_cbranch_scc0 .Lattp
	s_setprio 1

; #define LAS __attribute__((address_space(3)))
; __device__ __forceinline__ int opaque_tid() { int t = threadIdx.x; asm volatile("" : "+v"(t)); return t; }
; __device__ __forceinline__ unsigned char* opaque_ptr(unsigned char* q) { long z = 0; asm volatile("" : "+s"(z)); return q + z; }
;     __device__ __forceinline__ void init(const void* A_, const void* B_, int G_, int c_) { T.init(A_, B_, DM, DM, NLAT / 256, INP / 256, 1, 0, 0, G_, c_, 0); }
; __device__ __forceinline__ void sgu_unit(const Params& p, int l, int un, LAS unsigned char* lds) {
;     const int tid = opaque_tid(), lane = tid & 63, wave = tid >> 6;
;     unsigned char* ws = opaque_ptr(p.ws);
;     const bf16_t* P = (const bf16_t*)(ws + WS_PA);
;     bf16_t* CAT = (bf16_t*)(ws + WS_CAT);
;     const int cc = un >> 2, h = un & 3; const int row0 = cc * 128;
;     LAS bf16_t* Wl = (LAS bf16_t*)lds;
;     LAS bf16_t* Vl = (LAS bf16_t*)(lds + 128 * 136 * 2);
;     const float* Wg = p.in[I_SGUW] + ((size_t)l * 4 + h) * 128 * 128;
;     f32x4 wq[8]; u32x4 vv[16];
; #pragma unroll
;     for (int i = 0; i < 8; ++i) wq[i] = *(const f32x4*)(Wg + (i * 512 + tid) * 4);
; #pragma unroll
;     for (int qi = 0; qi < 16; ++qi) vv[qi] = *(const u32x4*)(P + (size_t)(row0 + wave * 16 + qi) * INP + C_SGU_V + lane * 8);
; __global__ void __launch_bounds__(512, 2) fwd(Params p) {
;     ...
;             ph_attn_carry(p, l, lds); __syncthreads();
;             { pg8::TileSched S; S.init(ws + WS_UPK, (bf16_t*)(ws + WS_G2B) + (size_t)l * 32 * 256 * 512, 512, 512, 3, 1, 32, (size_t)768 * 512 * 2, (size_t)256 * 512 * 2, G, c, (l == 0 && G == 256) ? 32 : 0);
;               pg8::EpiS2 E{(bf16_t*)(ws + WS_GB)};
;               pg8::Unit u0; if (S.next(0, u0)) { carry_wait(p, l); pg8::gemm_phase(lds, pg8::Desc{512, 512, 512}, S, E); }
;               else if (G == 256) { const int un = c - (l == 0 ? 128 : 96); if (un >= 0) sgu_unit(p, l, un, lds); } }
.LBB0_1258:
	s_setprio 0
	v_readlane_b32 s0, v251, 50
	v_readlane_b32 s2, v252, 20
	v_readlane_b32 s1, v251, 51
	v_readlane_b32 s3, v252, 21
	s_and_b64 s[0:1], s[0:1], s[2:3]
	s_and_b64 s[0:1], s[0:1], exec
	s_cselect_b32 s0, 32, 0
	v_readlane_b32 s2, v255, 11
	s_mul_hi_u32 s1, s0, s2
	v_readlane_b32 s3, v255, 12
	s_mul_i32 s1, s1, s3
	s_sub_i32 s0, s0, s1
	s_sub_i32 s1, s0, s3
	s_cmp_ge_u32 s0, s3
	s_cselect_b32 s0, s1, s0
	s_sub_i32 s1, s0, s3
	s_cmp_ge_u32 s0, s3
	s_cselect_b32 s0, s1, s0
	v_readlane_b32 s1, v255, 42
	s_sub_i32 s0, s1, s0
	s_ashr_i32 s1, s0, 31
	s_abs_i32 s0, s0
	s_mul_hi_u32 s2, s0, s2
	s_mul_i32 s2, s2, s3
	s_sub_i32 s0, s0, s2
	s_sub_i32 s2, s0, s3
	s_cmp_ge_u32 s0, s3
	s_cselect_b32 s0, s2, s0
	s_sub_i32 s2, s0, s3
	s_cmp_ge_u32 s0, s3
	s_cselect_b32 s0, s2, s0
	s_xor_b32 s0, s0, s1
	s_sub_i32 s26, s0, s1
	s_cmpk_gt_i32 s26, 0x5f
	s_mov_b64 s[0:1], -1
	s_barrier
	s_cbranch_scc0 .LBB0_1294
	v_readlane_b32 s0, v252, 20
	v_readlane_b32 s1, v252, 21
	s_and_b64 s[0:1], s[0:1], exec
	s_movk_i32 s0, 0xff80
	s_cselect_b32 s0, s0, 0xffffffa0
	s_add_i32 s0, s0, s92
	v_readlane_b32 s12, v251, 50
	s_cmp_lt_i32 s0, 0
	v_readlane_b32 s13, v251, 51
	s_cselect_b64 s[2:3], -1, 0
	s_xor_b64 s[12:13], s[12:13], -1
	s_or_b64 s[2:3], s[2:3], s[12:13]
	s_and_b64 vcc, exec, s[2:3]
	s_cbranch_vccnz .LBB0_1293
	v_readlane_b32 s2, v252, 5
	v_readlane_b32 s44, v251, 16
	s_lshl_b32 s1, s0, 5
	s_lshl_b32 s0, s2, 9
	v_readlane_b32 s2, v253, 39
	v_readlane_b32 s48, v251, 20
	v_readlane_b32 s49, v251, 21
	v_readlane_b32 s3, v252, 6
	s_or_b32 s40, s0, s2
	s_mov_b32 s41, s5
	v_readlane_b32 s50, v251, 22
	v_readlane_b32 s51, v251, 23
	v_readlane_b32 s52, v251, 24
	v_readlane_b32 s53, v251, 25
	v_readlane_b32 s54, v251, 26
	v_readlane_b32 s55, v251, 27
	s_mov_b64 s[12:13], s[48:49]
	s_lshl_b64 s[2:3], s[40:41], 9
	s_mov_b64 s[14:15], s[50:51]
	v_mov_b32_e32 v64, v0
	s_add_u32 s2, s14, s2
	s_addc_u32 s3, s15, s3
	v_lshlrev_b32_e32 v2, 2, v64
	v_ashrrev_i32_e32 v3, 31, v2
	v_add_u32_e32 v62, 0x800, v2
	s_mov_b64 s[14:15], 0
	v_lshl_add_u64 v[4:5], v[2:3], 2, s[2:3]
	v_ashrrev_i32_e32 v63, 31, v62
	v_lshl_add_u64 v[6:7], v[62:63], 2, s[2:3]
	global_load_dwordx4 v[66:69], v[4:5], off
	global_load_dwordx4 v[70:73], v[6:7], off
	v_add_u32_e32 v102, 0x1000, v2
	v_ashrrev_i32_e32 v103, 31, v102
	v_add_u32_e32 v104, 0x1800, v2
	v_lshl_add_u64 v[4:5], v[102:103], 2, s[2:3]
	v_ashrrev_i32_e32 v105, 31, v104
	s_and_b32 s12, s1, 0x7fffff80
	s_mov_b32 s1, s5
	v_lshl_add_u64 v[6:7], v[104:105], 2, s[2:3]
	global_load_dwordx4 v[74:77], v[4:5], off
	global_load_dwordx4 v[78:81], v[6:7], off
	s_lshl_b64 s[0:1], s[0:1], 2
	v_readlane_b32 s13, v253, 41
	v_add_u32_e32 v106, 0x2000, v2
	s_add_u32 s0, s13, s0
	v_readlane_b32 s13, v253, 42
	v_ashrrev_i32_e32 v107, 31, v106
	v_add_u32_e32 v108, 0x2800, v2
	s_addc_u32 s1, s13, s1
	v_lshl_add_u64 v[4:5], v[106:107], 2, s[2:3]
	v_ashrrev_i32_e32 v109, 31, v108
	s_add_u32 s36, s84, s14
	v_lshl_add_u64 v[6:7], v[108:109], 2, s[2:3]
	global_load_dwordx4 v[82:85], v[4:5], off
	global_load_dwordx4 v[86:89], v[6:7], off
	s_addc_u32 s37, s85, s15
	v_add_u32_e32 v110, 0x3000, v2
	v_add_u32_e32 v112, 0x3800, v2
	s_add_u32 s38, s36, 0x1f1b8000
	v_ashrrev_i32_e32 v111, 31, v110
	v_ashrrev_i32_e32 v113, 31, v112
	v_ashrrev_i32_e32 v103, 6, v64
	s_addc_u32 s39, s37, 0
	v_lshl_add_u64 v[4:5], v[110:111], 2, s[2:3]
	v_lshl_add_u64 v[2:3], v[112:113], 2, s[2:3]
	v_lshlrev_b32_e32 v65, 4, v103
	v_and_b32_e32 v8, 63, v64
	global_load_dwordx4 v[90:93], v[4:5], off
	global_load_dwordx4 v[94:97], v[2:3], off
	v_add_u32_e32 v9, s12, v65
	v_mov_b64_e32 v[2:3], s[38:39]
	s_movk_i32 s13, 0x1e00
	v_mad_i64_i32 v[4:5], s[2:3], v9, s13, v[2:3]
	v_lshlrev_b32_e32 v206, 4, v8
	v_or_b32_e32 v6, 1, v9
	v_lshl_add_u64 v[4:5], v[4:5], 0, v[206:207]
	v_mad_i64_i32 v[6:7], s[2:3], v6, s13, v[2:3]
	v_lshl_add_u64 v[6:7], v[6:7], 0, v[206:207]
	global_load_dwordx4 v[98:101], v[4:5], off offset:1024
	global_load_dwordx4 v[58:61], v[6:7], off offset:1024
	v_or_b32_e32 v4, 2, v9
	v_or_b32_e32 v6, 3, v9
	v_mad_i64_i32 v[4:5], s[2:3], v4, s13, v[2:3]
	v_mad_i64_i32 v[6:7], s[2:3], v6, s13, v[2:3]
	v_lshl_add_u64 v[4:5], v[4:5], 0, v[206:207]
	v_lshl_add_u64 v[6:7], v[6:7], 0, v[206:207]
	global_load_dwordx4 v[54:57], v[4:5], off offset:1024
	global_load_dwordx4 v[50:53], v[6:7], off offset:1024
	v_or_b32_e32 v4, 4, v9
	v_or_b32_e32 v6, 5, v9
	v_mad_i64_i32 v[4:5], s[2:3], v4, s13, v[2:3]
	v_mad_i64_i32 v[6:7], s[2:3], v6, s13, v[2:3]
	v_lshl_add_u64 v[4:5], v[4:5], 0, v[206:207]
	v_lshl_add_u64 v[6:7], v[6:7], 0, v[206:207]
	global_load_dwordx4 v[46:49], v[4:5], off offset:1024
	global_load_dwordx4 v[42:45], v[6:7], off offset:1024
	v_or_b32_e32 v4, 6, v9
	v_or_b32_e32 v6, 7, v9
	v_mad_i64_i32 v[4:5], s[2:3], v4, s13, v[2:3]
	v_mad_i64_i32 v[6:7], s[2:3], v6, s13, v[2:3]
	v_lshl_add_u64 v[4:5], v[4:5], 0, v[206:207]
	v_lshl_add_u64 v[6:7], v[6:7], 0, v[206:207]
	global_load_dwordx4 v[38:41], v[4:5], off offset:1024
	global_load_dwordx4 v[34:37], v[6:7], off offset:1024
	v_or_b32_e32 v4, 8, v9
	v_or_b32_e32 v6, 9, v9
	v_mad_i64_i32 v[4:5], s[2:3], v4, s13, v[2:3]
	v_mad_i64_i32 v[6:7], s[2:3], v6, s13, v[2:3]
	v_lshl_add_u64 v[4:5], v[4:5], 0, v[206:207]
	v_lshl_add_u64 v[6:7], v[6:7], 0, v[206:207]
	global_load_dwordx4 v[30:33], v[4:5], off offset:1024
	global_load_dwordx4 v[26:29], v[6:7], off offset:1024
	v_or_b32_e32 v4, 10, v9
	v_or_b32_e32 v6, 11, v9
	v_mad_i64_i32 v[4:5], s[2:3], v4, s13, v[2:3]
	v_mad_i64_i32 v[6:7], s[2:3], v6, s13, v[2:3]
	v_lshl_add_u64 v[4:5], v[4:5], 0, v[206:207]
	v_lshl_add_u64 v[6:7], v[6:7], 0, v[206:207]
	global_load_dwordx4 v[22:25], v[4:5], off offset:1024
	global_load_dwordx4 v[18:21], v[6:7], off offset:1024
	v_or_b32_e32 v4, 12, v9
	v_or_b32_e32 v6, 13, v9
	v_mad_i64_i32 v[4:5], s[2:3], v4, s13, v[2:3]
	v_mad_i64_i32 v[6:7], s[2:3], v6, s13, v[2:3]
	v_lshl_add_u64 v[4:5], v[4:5], 0, v[206:207]
	v_lshl_add_u64 v[6:7], v[6:7], 0, v[206:207]
	v_lshlrev_b32_e32 v105, 3, v64
	global_load_dwordx4 v[14:17], v[4:5], off offset:1024
	global_load_dwordx4 v[10:13], v[6:7], off offset:1024
	v_or_b32_e32 v4, 14, v9
	v_or_b32_e32 v6, 15, v9
	v_and_b32_e32 v63, 0xf8, v105
	v_mad_i64_i32 v[4:5], s[2:3], v4, s13, v[2:3]
	v_mad_i64_i32 v[2:3], s[2:3], v6, s13, v[2:3]
	v_add_u32_e32 v114, 0, v63
	v_bfe_i32 v63, v64, 5, 25
	s_movk_i32 s13, 0x110
	v_lshl_add_u64 v[4:5], v[4:5], 0, v[206:207]
	v_lshl_add_u64 v[2:3], v[2:3], 0, v[206:207]
	s_waitcnt vmcnt(21)
; #define LAS __attribute__((address_space(3)))
; __device__ __forceinline__ unsigned cvt_pk_bf16(float lo, float hi) { const f32x2 v = {lo, hi}; const bf16x2_t b = __builtin_convertvector(v, bf16x2_t); return __builtin_bit_cast(unsigned, b); }
; __device__ __forceinline__ float bflo(unsigned w) { return __uint_as_float(w << 16); }
; __device__ __forceinline__ float bfhi(unsigned w) { return __uint_as_float(w & 0xffff0000u); }
; __device__ __forceinline__ void sgu_unit(const Params& p, int l, int un, LAS unsigned char* lds) {
;     ...
;     for (int i = 0; i < 8; ++i) { const int e4 = (i * 512 + tid) * 4, r = e4 >> 7, c = e4 & 127; const f32x4 v = wq[i];
;         u32x2 w; w.x = cvt_pk_bf16(v[0], v[1]); w.y = cvt_pk_bf16(v[2], v[3]); *(LAS u32x2*)(Wl + r * 136 + c) = w; }
; #pragma unroll
;     for (int qi = 0; qi < 16; ++qi) { const int q = wave * 16 + qi;
;         const u32x4 v = vv[qi]; float f[8] = {bflo(v.x), bfhi(v.x), bflo(v.y), bfhi(v.y), bflo(v.z), bfhi(v.z), bflo(v.w), bfhi(v.w)}; float ss = 0.f;
; #pragma unroll
;         for (int j = 0; j < 8; ++j) { f[j] = gelu_tanh(f[j]); ss += f[j] * f[j]; }
;         ss = wave_sum(ss); const float rinv = rsqrtf(ss * (1.0f / 512.0f) + EPS);
;         if ((lane >> 4) == h) { const int c0 = (lane & 15) * 8; const float* g = p.in[I_SGUNG] + l * 512 + h * 128 + c0;
	v_cvt_pk_bf16_f32 v66, v66, v67
	v_cvt_pk_bf16_f32 v67, v68, v69
	v_mad_u64_u32 v[68:69], s[2:3], v63, s13, v[114:115]
	global_load_dwordx4 v[6:9], v[4:5], off offset:1024
	s_nop 0
	global_load_dwordx4 v[2:5], v[2:3], off offset:1024
	ds_write_b64 v68, v[66:67]
	v_ashrrev_i32_e32 v66, 7, v62
	s_waitcnt vmcnt(22)
	v_cvt_pk_bf16_f32 v62, v70, v71
	v_cvt_pk_bf16_f32 v63, v72, v73
	v_mad_u64_u32 v[66:67], s[2:3], v66, s13, v[114:115]
	ds_write_b64 v66, v[62:63]
	v_ashrrev_i32_e32 v66, 7, v102
	s_waitcnt vmcnt(21)
	v_cvt_pk_bf16_f32 v62, v74, v75
	v_cvt_pk_bf16_f32 v63, v76, v77
	v_mad_u64_u32 v[66:67], s[2:3], v66, s13, v[114:115]
	ds_write_b64 v66, v[62:63]
	v_ashrrev_i32_e32 v66, 7, v104
	s_waitcnt vmcnt(20)
	v_cvt_pk_bf16_f32 v62, v78, v79
	v_cvt_pk_bf16_f32 v63, v80, v81
	v_mad_u64_u32 v[66:67], s[2:3], v66, s13, v[114:115]
	ds_write_b64 v66, v[62:63]
	v_ashrrev_i32_e32 v66, 7, v106
	s_waitcnt vmcnt(19)
	v_cvt_pk_bf16_f32 v62, v82, v83
	v_cvt_pk_bf16_f32 v63, v84, v85
	v_mad_u64_u32 v[66:67], s[2:3], v66, s13, v[114:115]
	ds_write_b64 v66, v[62:63]
	v_ashrrev_i32_e32 v66, 7, v108
	s_waitcnt vmcnt(18)
	v_cvt_pk_bf16_f32 v62, v86, v87
	v_cvt_pk_bf16_f32 v63, v88, v89
	v_mad_u64_u32 v[66:67], s[2:3], v66, s13, v[114:115]
	ds_write_b64 v66, v[62:63]
	v_ashrrev_i32_e32 v66, 7, v110
	s_waitcnt vmcnt(17)
	v_cvt_pk_bf16_f32 v62, v90, v91
	v_cvt_pk_bf16_f32 v63, v92, v93
	v_mad_u64_u32 v[66:67], s[2:3], v66, s13, v[114:115]
	ds_write_b64 v66, v[62:63]
	v_ashrrev_i32_e32 v66, 7, v112
	v_mad_u64_u32 v[66:67], s[2:3], v66, s13, v[114:115]
	s_waitcnt vmcnt(15)
	v_and_b32_e32 v67, 0xffff0000, v98
	v_mul_f32_e32 v73, 0x3dd2d3e8, v67
	v_fma_f32 v73, -v73, v67, s33
	v_mul_f32_e32 v73, v73, v67
	v_exp_f32_e32 v73, v73
	v_cvt_pk_bf16_f32 v62, v94, v95
	v_cvt_pk_bf16_f32 v63, v96, v97
	ds_write_b64 v66, v[62:63]
	v_lshlrev_b32_e32 v66, 16, v98
	v_add_f32_e32 v73, 1.0, v73
	v_mul_f32_e32 v72, 0x3dd2d3e8, v66
	v_rcp_f32_e32 v73, v73
	v_fma_f32 v72, -v72, v66, s33
	v_mul_f32_e32 v72, v72, v66
	v_lshlrev_b32_e32 v69, 16, v99
	v_exp_f32_e32 v72, v72
	v_mul_f32_e32 v79, v73, v67
	v_mul_f32_e32 v67, 0x3dd2d3e8, v69
	v_fma_f32 v67, -v67, v69, s33
	v_mul_f32_e32 v67, v67, v69
	v_add_f32_e32 v72, 1.0, v72
	v_exp_f32_e32 v67, v67
	v_rcp_f32_e32 v72, v72
	v_lshlrev_b32_e32 v71, 16, v100
	v_and_b32_e32 v70, 0xffff0000, v99
	v_add_f32_e32 v67, 1.0, v67
	v_mul_f32_e32 v73, 0x3dd2d3e8, v71
	v_mul_f32_e32 v81, v72, v66
	v_mul_f32_e32 v72, 0x3dd2d3e8, v70
	v_rcp_f32_e32 v67, v67
	v_fma_f32 v73, -v73, v71, s33
	v_fma_f32 v72, -v72, v70, s33
	v_mul_f32_e32 v73, v73, v71
	v_mul_f32_e32 v72, v72, v70
	v_exp_f32_e32 v73, v73
	v_and_b32_e32 v74, 0xffff0000, v100
	v_exp_f32_e32 v72, v72
	v_mul_f32_e32 v80, v67, v69
	v_mul_f32_e32 v69, 0x3dd2d3e8, v74
	v_fma_f32 v69, -v69, v74, s33
	v_add_f32_e32 v67, 1.0, v73
	v_mul_f32_e32 v69, v69, v74
	v_add_f32_e32 v72, 1.0, v72
	v_rcp_f32_e32 v67, v67
	v_exp_f32_e32 v69, v69
	v_rcp_f32_e32 v72, v72
	v_lshlrev_b32_e32 v75, 16, v101
	v_and_b32_e32 v82, 0xffff0000, v101
	v_mul_f32_e32 v76, v67, v71
	v_add_f32_e32 v67, 1.0, v69
	v_mul_f32_e32 v69, 0x3dd2d3e8, v75
	v_mul_f32_e32 v78, v72, v70
	v_fma_f32 v69, -v69, v75, s33
	v_mul_f32_e32 v70, 0x3dd2d3e8, v82
	v_mul_f32_e32 v69, v69, v75
	v_fma_f32 v70, -v70, v82, s33
	v_rcp_f32_e32 v67, v67
	v_exp_f32_e32 v69, v69
	v_mul_f32_e32 v70, v70, v82
	v_exp_f32_e32 v70, v70
	v_mul_f32_e32 v66, v79, v79
	v_mul_f32_e32 v77, v67, v74
	v_add_f32_e32 v67, 1.0, v69
	v_fmac_f32_e32 v66, v81, v81
	v_rcp_f32_e32 v67, v67
	v_add_f32_e32 v69, 1.0, v70
	v_fmac_f32_e32 v66, v80, v80
	v_rcp_f32_e32 v69, v69
	v_and_b32_e32 v62, 64, v249
	v_fmac_f32_e32 v66, v78, v78
	v_add_u32_e32 v62, 64, v62
	v_xor_b32_e32 v63, 32, v249
	v_fmac_f32_e32 v66, v76, v76
	v_cmp_lt_i32_e32 vcc, v63, v62
	v_fmac_f32_e32 v66, v77, v77
	v_mul_f32_e32 v75, v67, v75
	v_cndmask_b32_e32 v63, v249, v63, vcc
	v_fmac_f32_e32 v66, v75, v75
	v_mul_f32_e32 v74, v69, v82
	v_lshlrev_b32_e32 v68, 2, v63
	v_fmac_f32_e32 v66, v74, v74
	v_mov_b32_e32 v67, v66
	s_nop 1
	v_permlane32_swap_b32_e32 v67, v66
	v_and_b32_e32 v84, 0x78, v105
	v_readlane_b32 s2, v253, 40
	s_waitcnt lgkmcnt(0)
	v_add_f32_e32 v66, v66, v67
	v_mov_b32_e32 v67, v66
	s_nop 1
	v_permlane16_swap_b32_e32 v67, v66
	v_lshlrev_b32_e32 v206, 2, v84
	v_readlane_b32 s45, v251, 17
	s_waitcnt lgkmcnt(0)
	v_add_f32_e32 v66, v66, v67
	s_nop 1
	v_mov_b32_dpp v67, v66 row_ror:8 row_mask:0xf bank_mask:0xf
	v_readlane_b32 s46, v251, 18
	v_readlane_b32 s47, v251, 19
	s_waitcnt lgkmcnt(0)
	v_add_f32_e32 v66, v66, v67
	s_nop 1
	v_mov_b32_dpp v67, v66 row_shl:4 row_mask:0xf bank_mask:0x5
	v_mov_b32_dpp v67, v66 row_shr:4 row_mask:0xf bank_mask:0xa
	v_readlane_b32 s56, v251, 28
	v_readlane_b32 s57, v251, 29
	v_readlane_b32 s58, v251, 30
	v_readlane_b32 s59, v251, 31
	s_waitcnt lgkmcnt(0)
	v_add_f32_e32 v63, v66, v67
	s_nop 1
	v_mov_b32_dpp v67, v63 quad_perm:[2,3,0,1] row_mask:0xf bank_mask:0xf
	v_bfe_u32 v66, v64, 4, 2
	v_cmp_eq_u32_e32 vcc, s2, v66
	s_mov_b64 s[16:17], s[52:53]
	s_waitcnt lgkmcnt(0)
	v_add_f32_e32 v82, v63, v67
	s_nop 1
	v_mov_b32_dpp v83, v82 quad_perm:[1,0,3,2] row_mask:0xf bank_mask:0xf
	v_lshl_add_u32 v67, v103, 5, 0
	v_lshl_add_u64 v[62:63], s[0:1], 0, v[206:207]
	v_mad_u32_u24 v67, v84, s13, v67
	v_lshrrev_b32_e32 v170, 6, v0
	v_lshlrev_b32_e32 v170, 1, v170
	v_and_b32_e32 v171, 15, v0
	v_xor_b32_e32 v168, v170, v171
	v_sub_u32_e32 v168, v168, v170
	v_lshl_add_u32 v168, v168, 4, v67
	v_or_b32_e32 v170, 1, v170
	v_xor_b32_e32 v169, v170, v171
	v_sub_u32_e32 v169, v169, v170
	v_lshl_add_u32 v169, v169, 4, v67
	s_mov_b64 s[18:19], s[54:55]
	s_and_saveexec_b64 s[0:1], vcc
	s_cbranch_execz .LBB0_1262
; __device__ __forceinline__ unsigned short f2bf(float f) { return (unsigned short)(cvt_pk_bf16(f, 0.f) & 0xffffu); }
; __device__ __forceinline__ void sgu_unit(const Params& p, int l, int un, LAS unsigned char* lds) {
;     ...
;         ss = wave_sum(ss); const float rinv = rsqrtf(ss * (1.0f / 512.0f) + EPS);
;         if ((lane >> 4) == h) { const int c0 = (lane & 15) * 8; const float* g = p.in[I_SGUNG] + l * 512 + h * 128 + c0;
; #pragma unroll
;             for (int j = 0; j < 8; ++j) Vl[(c0 + j) * 136 + q] = f2bf(f[j] * rinv * g[j]); } }
	s_waitcnt lgkmcnt(0)
	v_add_f32_e32 v82, v82, v83
	v_fmamk_f32 v82, v82, 0x3b000000, v246
	s_mov_b32 s2, 0x800000
	v_cmp_gt_f32_e64 s[2:3], s2, v82
	v_mul_f32_e32 v83, 0x4b800000, v82
	s_nop 0
	v_cndmask_b32_e64 v82, v82, v83, s[2:3]
	v_rsq_f32_e32 v82, v82
	s_nop 0
	v_mul_f32_e32 v83, 0x45800000, v82
	v_cndmask_b32_e64 v90, v82, v83, s[2:3]
	global_load_dwordx4 v[82:85], v[62:63], off offset:16
	global_load_dwordx4 v[86:89], v[62:63], off
	v_mul_f32_e32 v79, v79, v90
	v_mul_f32_e32 v76, v76, v90
	v_mul_f32_e32 v81, v81, v90
	v_mul_f32_e32 v78, v78, v90
	v_mul_f32_e32 v75, v75, v90
	v_mul_f32_e32 v74, v74, v90
	s_waitcnt vmcnt(1)
	v_mul_f32_e32 v76, v76, v82
	s_waitcnt vmcnt(0)
	v_mov_b32_e32 v160, v86
	v_mov_b32_e32 v161, v87
	v_mov_b32_e32 v162, v88
	v_mov_b32_e32 v163, v89
	v_mov_b32_e32 v164, v82
	v_mov_b32_e32 v165, v83
	v_mov_b32_e32 v166, v84
	v_mov_b32_e32 v167, v85
	v_mul_f32_e32 v79, v79, v87
	v_cvt_pk_bf16_f32 v79, v79, s0
	v_cvt_pk_bf16_f32 v76, v76, s0
	ds_write_b16 v168, v79 offset:35088
	v_mul_f32_e32 v79, v80, v90
	ds_write_b16 v168, v76 offset:35904
	v_mul_f32_e32 v76, v77, v90
	v_mul_f32_e32 v81, v81, v86
	v_mul_f32_e32 v79, v79, v88
	v_mul_f32_e32 v78, v78, v89
	v_mul_f32_e32 v76, v76, v83
	v_mul_f32_e32 v75, v75, v84
	v_mul_f32_e32 v74, v74, v85
	v_cvt_pk_bf16_f32 v81, v81, s0
	v_cvt_pk_bf16_f32 v79, v79, s0
	v_cvt_pk_bf16_f32 v78, v78, s0
	v_cvt_pk_bf16_f32 v76, v76, s0
	v_cvt_pk_bf16_f32 v75, v75, s0
	v_cvt_pk_bf16_f32 v74, v74, s0
	ds_write_b16 v168, v81 offset:34816
	ds_write_b16 v168, v79 offset:35360
	ds_write_b16 v168, v78 offset:35632
	ds_write_b16 v168, v76 offset:36176
	ds_write_b16 v168, v75 offset:36448
	ds_write_b16 v168, v74 offset:36720
